# baseline (speedup 1.0000x reference)
.LBB2_22:
	s_and_b64 vcc, exec, s[4:5]
	s_cbranch_vccz .LBB2_275
	s_load_dwordx2 s[8:9], s[0:1], 0x10
	s_load_dwordx2 s[98:99], s[0:1], 0x0
	s_movk_i32 s3, 0xc4
	v_cmp_gt_u32_e32 vcc, s3, v0
	v_mov_b32_e32 v4, 0
	v_mov_b32_e32 v1, 0
	s_and_saveexec_b64 s[4:5], vcc
	s_cbranch_execz .LBB2_25
	v_lshlrev_b32_e32 v1, 8, v0
	s_waitcnt lgkmcnt(0)
	global_load_dword v1, v1, s[8:9]

.LBB2_27:
	s_or_b64 exec, exec, s[4:5]
	s_lshr_b32 s96, s2, 1
	s_lshl_b32 s96, s96, 8
	s_and_b32 s97, s2, 1
	s_lshl_b32 s97, s97, 2
	s_add_u32 s96, s96, s97
	s_waitcnt lgkmcnt(0)
	s_load_dword s100, s[8:9], s96
	s_mul_i32 s101, s2, 0x6000
	s_add_u32 s98, s98, s101
	s_addc_u32 s99, s99, 0
	v_lshlrev_b32_e32 v100, 2, v0
	v_add_u32_e32 v101, 0x1000, v100
	v_add_u32_e32 v102, 0x2000, v100
	v_add_u32_e32 v103, 0x3000, v100
	v_add_u32_e32 v104, 0x4000, v100
	v_add_u32_e32 v105, 0x5000, v100
	s_waitcnt lgkmcnt(0)
	s_min_i32 s100, s100, 0x1800
	v_cmp_gt_i32_e32 vcc, s100, v0
	s_and_saveexec_b64 s[4:5], vcc
	global_load_dword v76, v100, s[98:99]
	s_mov_b64 exec, s[4:5]
	v_add_u32_e32 v106, 0x100, v0
	v_cmp_gt_i32_e32 vcc, s100, v106
	s_and_saveexec_b64 s[4:5], vcc
	global_load_dword v77, v100, s[98:99] offset:1024
	s_mov_b64 exec, s[4:5]
	v_add_u32_e32 v106, 0x200, v0
	v_cmp_gt_i32_e32 vcc, s100, v106
	s_and_saveexec_b64 s[4:5], vcc
	global_load_dword v78, v100, s[98:99] offset:2048
	s_mov_b64 exec, s[4:5]
	v_add_u32_e32 v106, 0x300, v0
	v_cmp_gt_i32_e32 vcc, s100, v106
	s_and_saveexec_b64 s[4:5], vcc
	global_load_dword v79, v100, s[98:99] offset:3072
	s_mov_b64 exec, s[4:5]
	v_add_u32_e32 v106, 0x400, v0
	v_cmp_gt_i32_e32 vcc, s100, v106
	s_and_saveexec_b64 s[4:5], vcc
	global_load_dword v80, v101, s[98:99]
	s_mov_b64 exec, s[4:5]
	v_add_u32_e32 v106, 0x500, v0
	v_cmp_gt_i32_e32 vcc, s100, v106
	s_and_saveexec_b64 s[4:5], vcc
	global_load_dword v81, v101, s[98:99] offset:1024
	s_mov_b64 exec, s[4:5]
	v_add_u32_e32 v106, 0x600, v0
	v_cmp_gt_i32_e32 vcc, s100, v106
	s_and_saveexec_b64 s[4:5], vcc
	global_load_dword v82, v101, s[98:99] offset:2048
	s_mov_b64 exec, s[4:5]
	v_add_u32_e32 v106, 0x700, v0
	v_cmp_gt_i32_e32 vcc, s100, v106
	s_and_saveexec_b64 s[4:5], vcc
	global_load_dword v83, v101, s[98:99] offset:3072
	s_mov_b64 exec, s[4:5]
	v_add_u32_e32 v106, 0x800, v0
	v_cmp_gt_i32_e32 vcc, s100, v106
	s_and_saveexec_b64 s[4:5], vcc
	global_load_dword v84, v102, s[98:99]
	s_mov_b64 exec, s[4:5]
	v_add_u32_e32 v106, 0x900, v0
	v_cmp_gt_i32_e32 vcc, s100, v106
	s_and_saveexec_b64 s[4:5], vcc
	global_load_dword v85, v102, s[98:99] offset:1024
	s_mov_b64 exec, s[4:5]
	v_add_u32_e32 v106, 0xa00, v0
	v_cmp_gt_i32_e32 vcc, s100, v106
	s_and_saveexec_b64 s[4:5], vcc
	global_load_dword v86, v102, s[98:99] offset:2048
	s_mov_b64 exec, s[4:5]
	v_add_u32_e32 v106, 0xb00, v0
	v_cmp_gt_i32_e32 vcc, s100, v106
	s_and_saveexec_b64 s[4:5], vcc
	global_load_dword v87, v102, s[98:99] offset:3072
	s_mov_b64 exec, s[4:5]
	v_add_u32_e32 v106, 0xc00, v0
	v_cmp_gt_i32_e32 vcc, s100, v106
	s_and_saveexec_b64 s[4:5], vcc
	global_load_dword v88, v103, s[98:99]
	s_mov_b64 exec, s[4:5]
	v_add_u32_e32 v106, 0xd00, v0
	v_cmp_gt_i32_e32 vcc, s100, v106
	s_and_saveexec_b64 s[4:5], vcc
	global_load_dword v89, v103, s[98:99] offset:1024
	s_mov_b64 exec, s[4:5]
	v_add_u32_e32 v106, 0xe00, v0
	v_cmp_gt_i32_e32 vcc, s100, v106
	s_and_saveexec_b64 s[4:5], vcc
	global_load_dword v90, v103, s[98:99] offset:2048
	s_mov_b64 exec, s[4:5]
	v_add_u32_e32 v106, 0xf00, v0
	v_cmp_gt_i32_e32 vcc, s100, v106
	s_and_saveexec_b64 s[4:5], vcc
	global_load_dword v91, v103, s[98:99] offset:3072
	s_mov_b64 exec, s[4:5]
	v_add_u32_e32 v106, 0x1000, v0
	v_cmp_gt_i32_e32 vcc, s100, v106
	s_and_saveexec_b64 s[4:5], vcc
	global_load_dword v92, v104, s[98:99]
	s_mov_b64 exec, s[4:5]
	v_add_u32_e32 v106, 0x1100, v0
	v_cmp_gt_i32_e32 vcc, s100, v106
	s_and_saveexec_b64 s[4:5], vcc
	global_load_dword v93, v104, s[98:99] offset:1024
	s_mov_b64 exec, s[4:5]
	v_add_u32_e32 v106, 0x1200, v0
	v_cmp_gt_i32_e32 vcc, s100, v106
	s_and_saveexec_b64 s[4:5], vcc
	global_load_dword v94, v104, s[98:99] offset:2048
	s_mov_b64 exec, s[4:5]
	v_add_u32_e32 v106, 0x1300, v0
	v_cmp_gt_i32_e32 vcc, s100, v106
	s_and_saveexec_b64 s[4:5], vcc
	global_load_dword v95, v104, s[98:99] offset:3072
	s_mov_b64 exec, s[4:5]
	v_add_u32_e32 v106, 0x1400, v0
	v_cmp_gt_i32_e32 vcc, s100, v106
	s_and_saveexec_b64 s[4:5], vcc
	global_load_dword v96, v105, s[98:99]
	s_mov_b64 exec, s[4:5]
	v_add_u32_e32 v106, 0x1500, v0
	v_cmp_gt_i32_e32 vcc, s100, v106
	s_and_saveexec_b64 s[4:5], vcc
	global_load_dword v97, v105, s[98:99] offset:1024
	s_mov_b64 exec, s[4:5]
	v_add_u32_e32 v106, 0x1600, v0
	v_cmp_gt_i32_e32 vcc, s100, v106
	s_and_saveexec_b64 s[4:5], vcc
	global_load_dword v98, v105, s[98:99] offset:2048
	s_mov_b64 exec, s[4:5]
	v_add_u32_e32 v106, 0x1700, v0
	v_cmp_gt_i32_e32 vcc, s100, v106
	s_and_saveexec_b64 s[4:5], vcc
	global_load_dword v99, v105, s[98:99] offset:3072
	s_mov_b64 exec, s[4:5]
	v_lshlrev_b32_e32 v8, 2, v0
	s_waitcnt vmcnt(0)
	v_add_u32_e32 v4, v4, v1
	v_mov_b32_e32 v5, 0
	v_cmp_ne_u32_e32 vcc, 0, v0
	v_add_u32_e32 v51, -4, v8
	v_mov_b32_e32 v6, 0
	ds_write_b32 v8, v4
	s_waitcnt lgkmcnt(0)
	s_barrier
	s_and_saveexec_b64 s[4:5], vcc
	ds_read_b32 v6, v51
	s_or_b64 exec, exec, s[4:5]
	s_waitcnt lgkmcnt(0)
	s_barrier
	ds_read_b32 v7, v8
	v_cmp_lt_u32_e64 s[52:53], 1, v0
	v_add_u32_e32 v52, -8, v8
	s_waitcnt lgkmcnt(0)
	v_add_u32_e32 v6, v7, v6
	ds_write_b32 v8, v6
	s_waitcnt lgkmcnt(0)
	s_barrier
	s_and_saveexec_b64 s[4:5], s[52:53]
	ds_read_b32 v5, v52
	s_or_b64 exec, exec, s[4:5]
	s_waitcnt lgkmcnt(0)
	s_barrier
	ds_read_b32 v6, v8
	v_cmp_lt_u32_e64 s[54:55], 3, v0
	v_add_u32_e32 v53, -16, v8
	s_waitcnt lgkmcnt(0)
	v_add_u32_e32 v5, v6, v5
	ds_write_b32 v8, v5
	v_mov_b32_e32 v5, 0
	v_mov_b32_e32 v6, 0
	s_waitcnt lgkmcnt(0)
	s_barrier
	s_and_saveexec_b64 s[4:5], s[54:55]
	ds_read_b32 v6, v53
	s_or_b64 exec, exec, s[4:5]
	s_waitcnt lgkmcnt(0)
	s_barrier
	ds_read_b32 v7, v8
	v_cmp_lt_u32_e64 s[56:57], 7, v0
	v_subrev_u32_e32 v54, 32, v8
	s_waitcnt lgkmcnt(0)
	v_add_u32_e32 v6, v7, v6
	ds_write_b32 v8, v6
	s_waitcnt lgkmcnt(0)
	s_barrier
	s_and_saveexec_b64 s[4:5], s[56:57]
	ds_read_b32 v5, v54
	s_or_b64 exec, exec, s[4:5]
	s_waitcnt lgkmcnt(0)
	s_barrier
	ds_read_b32 v6, v8
	v_cmp_lt_u32_e64 s[58:59], 15, v0
	v_subrev_u32_e32 v55, 64, v8
	s_waitcnt lgkmcnt(0)
	v_add_u32_e32 v5, v6, v5
	ds_write_b32 v8, v5
	v_mov_b32_e32 v5, 0
	v_mov_b32_e32 v6, 0
	s_waitcnt lgkmcnt(0)
	s_barrier
	s_and_saveexec_b64 s[4:5], s[58:59]
	ds_read_b32 v6, v55
	s_or_b64 exec, exec, s[4:5]
	s_waitcnt lgkmcnt(0)
	s_barrier
	ds_read_b32 v7, v8
	v_cmp_lt_u32_e64 s[60:61], 31, v0
	s_waitcnt lgkmcnt(0)
	v_add_u32_e32 v6, v7, v6
	ds_write_b32 v8, v6
	s_waitcnt lgkmcnt(0)
	s_barrier
	s_and_saveexec_b64 s[4:5], s[60:61]
	v_add_u32_e32 v5, 0xffffff80, v8
	ds_read_b32 v5, v5
	s_or_b64 exec, exec, s[4:5]
	s_waitcnt lgkmcnt(0)
	s_barrier
	ds_read_b32 v6, v8
	v_cmp_lt_u32_e64 s[62:63], 63, v0
	s_waitcnt lgkmcnt(0)
	v_add_u32_e32 v5, v6, v5
	ds_write_b32 v8, v5
	v_mov_b32_e32 v5, 0
	v_mov_b32_e32 v6, 0
	s_waitcnt lgkmcnt(0)
	s_barrier
	s_and_saveexec_b64 s[4:5], s[62:63]
	v_add_u32_e32 v6, 0xffffff00, v8
	ds_read_b32 v6, v6
	s_or_b64 exec, exec, s[4:5]
	s_waitcnt lgkmcnt(0)
	s_barrier
	ds_read_b32 v7, v8
	s_movk_i32 s3, 0x7f
	v_cmp_lt_u32_e64 s[64:65], s3, v0
	s_waitcnt lgkmcnt(0)
	v_add_u32_e32 v6, v7, v6
	ds_write_b32 v8, v6
	s_waitcnt lgkmcnt(0)
	s_barrier
	s_and_saveexec_b64 s[4:5], s[64:65]
	v_add_u32_e32 v5, 0xfffffe00, v8
	ds_read_b32 v5, v5
	s_or_b64 exec, exec, s[4:5]
	s_waitcnt lgkmcnt(0)
	s_barrier
	ds_read_b32 v6, v8
	s_load_dwordx2 s[10:11], s[0:1], 0x0
	v_cmp_eq_u32_e64 s[6:7], s2, v2
	v_cmp_eq_u32_e64 s[4:5], s2, v3
	s_or_b64 s[12:13], s[6:7], s[4:5]
	s_waitcnt lgkmcnt(0)
	v_add_u32_e32 v5, v6, v5
	ds_write_b32 v8, v5
	s_waitcnt lgkmcnt(0)
	s_barrier
	ds_read_b32 v5, v8
	s_waitcnt lgkmcnt(0)
	s_barrier
	s_and_saveexec_b64 s[6:7], s[12:13]
	v_cndmask_b32_e64 v1, 0, v1, s[4:5]
	v_sub_u32_e32 v1, v1, v4
	v_add_u32_e32 v1, v1, v5
	v_mov_b32_e32 v2, 0
	ds_write_b32 v2, v1 offset:2048
	s_or_b64 exec, exec, s[6:7]
	s_lshr_b32 s80, s2, 1
	s_lshl_b32 s80, s80, 6
	s_and_b32 s81, s2, 1
	s_or_b32 s80, s80, s81
	s_mov_b32 s81, 0
	s_lshl_b64 s[4:5], s[80:81], 2
	s_add_u32 s4, s8, s4
	v_mov_b32_e32 v1, 0
	s_addc_u32 s5, s9, s5
	ds_write_b32 v8, v1 offset:1024
	s_waitcnt lgkmcnt(0)
	s_barrier
	s_load_dword s3, s[4:5], 0x0
	ds_read_b32 v2, v1 offset:2048
	s_waitcnt lgkmcnt(0)
	s_cmpk_lt_i32 s3, 0x1801
	s_cbranch_scc1 .LBB2_47
	s_load_dword s81, s[8:9], 0xc380
